# baseline (speedup 1.0000x reference)
_Z8k_layer1PKiS0_PKfS2_PK15HIP_vector_typeIjLj4EEPKDv8_DF16_S9_S2_S2_S2_PDF16_PfSB_:
	s_load_dwordx2 s[14:15], s[0:1], 0x48
	s_load_dwordx8 s[4:11], s[0:1], 0x28
	s_load_dwordx2 s[56:57], s[0:1], 0x0
	v_readfirstlane_b32 s13, v0
	s_lshr_b32 s12, s13, 6
	v_and_b32_e32 v178, 63, v0
	v_lshl_or_b32 v2, s12, 10, v178
	v_ashrrev_i32_e32 v3, 31, v2
	v_lshlrev_b64 v[4:5], 4, v[2:3]
	s_lshl_b32 s16, s2, 5
	s_lshl_b32 s17, s12, 3
	s_add_i32 s16, s16, s17
	v_min_i32_e32 v1, 8, v178
	v_add_u32_e32 v1, s16, v1
	v_min_i32_e32 v1, 0xc350, v1
	v_lshlrev_b32_e32 v1, 2, v1
	s_waitcnt lgkmcnt(0)
	global_load_dword v236, v1, s[56:57]
	v_min_i32_e32 v1, 8, v178
	s_addk_i32 s16, 0x4000
	v_add_u32_e32 v1, s16, v1
	v_min_i32_e32 v1, 0xc350, v1
	v_lshlrev_b32_e32 v1, 2, v1
	global_load_dword v239, v1, s[56:57]
	v_lshl_add_u64 v[6:7], s[6:7], 0, v[4:5]
	s_movk_i32 s3, 0x1000
	v_add_co_u32_e32 v8, vcc, s3, v6
	s_movk_i32 s6, 0x2000
	s_nop 0
	v_addc_co_u32_e32 v9, vcc, 0, v7, vcc
	v_add_co_u32_e32 v10, vcc, s6, v6
	s_movk_i32 s6, 0x3000
	s_nop 0
	v_addc_co_u32_e32 v11, vcc, 0, v7, vcc
	global_load_dwordx4 v[32:35], v[6:7], off
	global_load_dwordx4 v[36:39], v[6:7], off offset:1024
	global_load_dwordx4 v[40:43], v[6:7], off offset:2048
	global_load_dwordx4 v[44:47], v[6:7], off offset:3072
	v_add_co_u32_e32 v6, vcc, s6, v6
	v_lshl_add_u64 v[4:5], s[4:5], 0, v[4:5]
	s_nop 0
	v_addc_co_u32_e32 v7, vcc, 0, v7, vcc
	v_or_b32_e32 v2, 0x200, v2
	global_load_dwordx4 v[48:51], v[8:9], off offset:1024
	global_load_dwordx4 v[52:55], v[8:9], off offset:2048
	global_load_dwordx4 v[56:59], v[10:11], off offset:-4096
	global_load_dwordx4 v[60:63], v[10:11], off
	global_load_dwordx4 v[64:67], v[10:11], off offset:1024
	global_load_dwordx4 v[68:71], v[10:11], off offset:2048
	global_load_dwordx4 v[72:75], v[10:11], off offset:3072
	global_load_dwordx4 v[76:79], v[8:9], off offset:3072
	global_load_dwordx4 v[80:83], v[6:7], off
	global_load_dwordx4 v[84:87], v[6:7], off offset:1024
	global_load_dwordx4 v[88:91], v[6:7], off offset:2048
	global_load_dwordx4 v[92:95], v[6:7], off offset:3072
	v_add_co_u32_e32 v6, vcc, s3, v4
	v_ashrrev_i32_e32 v3, 31, v2
	s_nop 0
	v_addc_co_u32_e32 v7, vcc, 0, v5, vcc
	v_lshl_add_u64 v[2:3], v[2:3], 4, s[4:5]
	global_load_dwordx4 v[96:99], v[4:5], off
	global_load_dwordx4 v[100:103], v[4:5], off offset:1024
	global_load_dwordx4 v[104:107], v[4:5], off offset:2048
	global_load_dwordx4 v[108:111], v[4:5], off offset:3072
	global_load_dwordx4 v[112:115], v[6:7], off
	global_load_dwordx4 v[116:119], v[6:7], off offset:1024
	global_load_dwordx4 v[120:123], v[6:7], off offset:2048
	global_load_dwordx4 v[124:127], v[6:7], off offset:3072
	global_load_dwordx4 v[128:131], v[2:3], off
	global_load_dwordx4 v[132:135], v[2:3], off offset:1024
	global_load_dwordx4 v[136:139], v[2:3], off offset:2048
	global_load_dwordx4 v[140:143], v[2:3], off offset:3072
	v_add_co_u32_e32 v2, vcc, s6, v4
	s_lshl_b32 s3, s12, 4
	s_nop 0
	v_addc_co_u32_e32 v3, vcc, 0, v5, vcc
	global_load_dwordx4 v[144:147], v[2:3], off
	global_load_dwordx4 v[148:151], v[2:3], off offset:1024
	global_load_dwordx4 v[152:155], v[2:3], off offset:2048
	global_load_dwordx4 v[156:159], v[2:3], off offset:3072
	v_and_or_b32 v1, v0, 15, s3
	v_lshlrev_b32_e32 v1, 2, v1
	global_load_dword v179, v1, s[10:11]
	global_load_dword v180, v1, s[14:15]
	v_bfe_u32 v2, v0, 4, 2
	s_lshl_b32 s16, s3, 2
	v_lshl_add_u32 v2, v2, 4, s16
	global_load_dwordx4 v[228:231], v2, s[10:11]
	global_load_dwordx4 v[232:235], v2, s[14:15]
	v_cmp_gt_u32_e32 vcc, 32, v0
	v_lshlrev_b32_e32 v0, 2, v0
	s_and_saveexec_b64 s[4:5], vcc
	v_mov_b32_e32 v1, 0
	v_add_u32_e32 v2, 0xd000, v0
	ds_write2_b32 v2, v1, v1 offset0:176 offset1:208
	s_or_b64 exec, exec, s[4:5]
	global_load_dword v1, v0, s[8:9]
	global_load_dword v2, v0, s[8:9] offset:1024
	s_cmpk_gt_i32 s2, 0x61a
	s_waitcnt vmcnt(0)
	ds_write2st64_b32 v0, v1, v2 offset0:202 offset1:206
	s_waitcnt lgkmcnt(0)
	s_barrier
	s_cbranch_scc1 .LBB3_271
	s_load_dwordx8 s[56:63], s[0:1], 0x0
	s_load_dwordx4 s[4:7], s[0:1], 0x50
	s_mul_i32 s87, s12, 48
	s_lshl_b32 s66, s12, 9
	s_and_b32 s65, s13, 0xffffffc0
	s_lshl_b32 s86, s12, 3
	s_waitcnt lgkmcnt(0)
	v_writelane_b32 v226, s4, 0
	s_add_i32 s87, s87, 0xd200
	s_add_i32 s90, s66, 0xc200
	v_writelane_b32 v226, s5, 1
	v_writelane_b32 v226, s6, 2
	v_writelane_b32 v226, s7, 3
	s_lshl_b32 s4, s12, 12
	s_add_i32 s88, s4, 0x8200
	s_lshl_b32 s5, s12, 1
	s_load_dwordx2 s[72:73], s[0:1], 0x20
	s_load_dwordx2 s[76:77], s[0:1], 0x60
	s_add_u32 s0, s0, 0x68
	s_addc_u32 s1, s1, 0
	v_mbcnt_lo_u32_b32 v0, -1, 0
	v_writelane_b32 v226, s0, 4
	v_mbcnt_hi_u32_b32 v182, -1, v0
	s_mul_i32 s99, s12, 0x2080
	v_writelane_b32 v226, s1, 5
	s_or_b32 s0, s5, 1
	v_and_b32_e32 v0, 64, v182
	s_mov_b32 s91, 0xff800000
	s_lshl_b32 s95, s12, 8
	s_lshl_b32 s64, s0, 8
	s_lshl_b32 s98, s0, 7
	s_add_i32 s93, s4, 0x8500
	s_or_b32 s92, s99, 48
	s_mov_b32 s68, 0
	v_mov_b32_e32 v177, 0
	v_mov_b32_e32 v181, 0xff800000
	s_movk_i32 s69, 0x410
	v_xor_b32_e32 v183, 32, v182
	v_add_u32_e32 v184, 64, v0
	v_xor_b32_e32 v185, 4, v182
	v_xor_b32_e32 v186, 8, v182
	v_xor_b32_e32 v187, 16, v182
	v_mov_b32_e32 v188, 0x3c0
	v_writelane_b32 v226, s92, 6
	s_branch .LBB3_6

.LBB3_6:
	v_mov_b32_e32 v189, v178
	s_lshl_b32 s74, s2, 5
	s_add_i32 s22, s74, s86
	v_mov_b32_e32 v0, v236
	v_readlane_b32 s0, v239, 0
	v_readlane_b32 s1, v239, 8
	v_mov_b32_e32 v236, v239
	s_sub_i32 s1, s1, s0
	s_add_i32 s1, s1, -1
	v_ashrrev_i32_e32 v240, 1, v189
	v_add_u32_e32 v244, 32, v240
	v_add_u32_e32 v248, 64, v240
	v_add_u32_e32 v252, 0x60, v240
	v_min_i32_e32 v240, s1, v240
	v_min_i32_e32 v244, s1, v244
	v_min_i32_e32 v248, s1, v248
	v_min_i32_e32 v252, s1, v252
	v_add_lshl_u32 v240, v240, s0, 2
	v_add_lshl_u32 v244, v244, s0, 2
	v_add_lshl_u32 v248, v248, s0, 2
	v_add_lshl_u32 v252, v252, s0, 2
	global_load_dword v240, v240, s[58:59]
	global_load_dword v244, v244, s[58:59]
	global_load_dword v248, v248, s[58:59]
	global_load_dword v252, v252, s[58:59]
	s_add_i32 s0, s2, 0x400
	s_lshl_b32 s0, s0, 5
	s_add_i32 s0, s0, s86
	v_min_i32_e32 v1, 8, v189
	v_add_u32_e32 v1, s0, v1
	v_min_i32_e32 v1, 0xc350, v1
	v_lshlrev_b32_e32 v1, 2, v1
	global_load_dword v239, v1, s[56:57]
	v_cmp_gt_i32_e32 vcc, 9, v189
	s_and_saveexec_b64 s[0:1], vcc
	s_cbranch_execz .LBB3_8
	v_lshl_add_u32 v1, v189, 2, s87
	ds_write_b32 v1, v0

.LBB3_86:
	s_and_b64 vcc, exec, s[0:1]
	s_cbranch_vccz .LBB3_222
	s_cmpk_ge_i32 s2, 0x200
	s_cbranch_scc1 .Lk4_staged
	v_ashrrev_i32_e32 v10, 3, v189
	v_add_u32_e32 v10, s22, v10
	v_min_i32_e32 v10, 0xc34f, v10
	v_and_b32_e32 v11, 7, v189
	v_lshl_or_b32 v176, v10, 3, v11
	v_lshl_add_u64 v[10:11], v[176:177], 2, s[62:63]
	global_load_dword v227, v[10:11], off
	v_ashrrev_i32_e32 v0, 1, v189
	s_add_i32 s79, s23, -1
	v_add_u32_e32 v5, 32, v0
	v_add_u32_e32 v7, 64, v0
	v_add_u32_e32 v2, 0x60, v0
	v_min_i32_e32 v9, s79, v0
	v_min_i32_e32 v5, s79, v5
	v_min_i32_e32 v7, s79, v7
	v_min_i32_e32 v2, s79, v2
	v_add_lshl_u32 v9, v9, s78, 2
	v_add_lshl_u32 v5, v5, s78, 2
	v_add_lshl_u32 v7, v7, s78, 2
	v_add_lshl_u32 v2, v2, s78, 2
	global_load_dword v9, v9, s[58:59]
	global_load_dword v5, v5, s[58:59]
	global_load_dword v7, v7, s[58:59]
	global_load_dword v2, v2, s[58:59]

.Lk4_staged:
	s_mov_b64 s[0:1], 0
.LBB3_111:
	s_or_b64 exec, exec, s[0:1]
	v_ashrrev_i32_e32 v167, 3, v189
	v_mov_b32_e32 v0, s87
	v_and_b32_e32 v169, -2, v167
	v_lshl_add_u32 v1, v167, 2, s87
	v_lshl_add_u32 v2, v169, 2, s87
	ds_read_b32 v0, v0
	ds_read_b32 v168, v2
	ds_read2_b32 v[160:161], v1 offset1:1
	v_subrev_u32_e32 v194, s78, v167
	s_add_i32 s79, s23, -1
	v_and_b32_e32 v193, 7, v189
	s_waitcnt lgkmcnt(0)
	v_add_u32_e32 v0, v194, v0
	v_min_i32_e32 v1, s79, v0
	v_add_u32_e32 v2, 8, v0
	v_add_u32_e32 v3, 16, v0
	v_add_u32_e32 v4, 24, v0
	v_min_i32_e32 v2, s79, v2
	v_min_i32_e32 v3, s79, v3
	v_min_i32_e32 v4, s79, v4
	v_lshl_add_u32 v1, v1, 2, s90
	v_lshl_add_u32 v2, v2, 2, s90
	v_lshl_add_u32 v3, v3, 2, s90
	v_lshl_add_u32 v4, v4, 2, s90
	ds_read_b32 v1, v1
	ds_read_b32 v2, v2
	ds_read_b32 v3, v3
	ds_read_b32 v4, v4
	s_waitcnt lgkmcnt(3)
	v_lshl_or_b32 v176, v1, 3, v193
	v_lshl_add_u64 v[20:21], v[176:177], 4, s[72:73]
	global_load_dwordx4 v[20:23], v[20:21], off
	s_waitcnt lgkmcnt(2)
	v_lshl_or_b32 v176, v2, 3, v193
	v_lshl_add_u64 v[16:17], v[176:177], 4, s[72:73]
	global_load_dwordx4 v[16:19], v[16:17], off
	s_waitcnt lgkmcnt(1)
	v_lshl_or_b32 v176, v3, 3, v193
	v_lshl_add_u64 v[28:29], v[176:177], 4, s[72:73]
	global_load_dwordx4 v[28:31], v[28:29], off
	s_waitcnt lgkmcnt(0)
	v_lshl_or_b32 v176, v4, 3, v193
	v_lshl_add_u64 v[24:25], v[176:177], 4, s[72:73]
	global_load_dwordx4 v[24:27], v[24:25], off

.LBB3_145:
	s_or_b64 exec, exec, s[54:55]
	v_rcp_f32_e32 v171, v163
	s_movk_i32 s69, 0x410
	v_lshlrev_b32_e32 v197, 6, v189
	v_fma_f32 v202, -v163, v171, 1.0
	v_fmac_f32_e32 v171, v202, v171
	v_cmp_lt_f32_e32 vcc, 0, v163
	v_mul_lo_u32 v169, v169, s69
	v_and_b32_e32 v197, 0x3c0, v197
	v_cndmask_b32_e32 v163, 0, v171, vcc
	v_sub_u32_e32 v171, v160, v168
	v_add3_u32 v201, s99, v169, v197
	s_max_i32 s32, s33, s96
	s_max_i32 s32, s32, s97
	s_max_i32 s32, s32, s75
	s_cmp_gt_i32 s32, 32
	s_cbranch_scc1 .Lk4_slowst
	s_and_saveexec_b64 s[54:55], s[44:45]
	v_lshl_add_u32 v238, v171, 1, v201
	v_fma_mixlo_f16 v225, v163, v225, 0
	ds_write_b16 v238, v225
	v_fma_mixlo_f16 v224, v163, v224, 0
	ds_write_b16 v238, v224 offset:2
	v_fma_mixlo_f16 v223, v163, v223, 0
	ds_write_b16 v238, v223 offset:4
	v_fma_mixlo_f16 v222, v163, v222, 0
	ds_write_b16 v238, v222 offset:6
	v_fma_mixlo_f16 v221, v163, v221, 0
	ds_write_b16 v238, v221 offset:8
	v_fma_mixlo_f16 v220, v163, v220, 0
	ds_write_b16 v238, v220 offset:10
	v_fma_mixlo_f16 v219, v163, v219, 0
	ds_write_b16 v238, v219 offset:12
	v_fma_mixlo_f16 v218, v163, v218, 0
	ds_write_b16 v238, v218 offset:14
	s_cmp_eq_u64 s[34:35], 0
	s_cbranch_scc1 .Lk4_stdone
	v_fma_mixlo_f16 v217, v163, v217, 0
	ds_write_b16 v238, v217 offset:16
	v_fma_mixlo_f16 v216, v163, v216, 0
	ds_write_b16 v238, v216 offset:18
	v_fma_mixlo_f16 v215, v163, v215, 0
	ds_write_b16 v238, v215 offset:20
	v_fma_mixlo_f16 v214, v163, v214, 0
	ds_write_b16 v238, v214 offset:22
	s_cmp_eq_u64 s[24:25], 0
	s_cbranch_scc1 .Lk4_stdone
	v_fma_mixlo_f16 v200, v163, v200, 0
	ds_write_b16 v238, v200 offset:24
	v_fma_mixlo_f16 v199, v163, v199, 0
	ds_write_b16 v238, v199 offset:26
	v_fma_mixlo_f16 v198, v163, v198, 0
	ds_write_b16 v238, v198 offset:28
	v_fma_mixlo_f16 v196, v163, v196, 0
	ds_write_b16 v238, v196 offset:30
	s_cmp_eq_u64 s[16:17], 0
	s_cbranch_scc1 .Lk4_stdone
	v_fma_mixlo_f16 v195, v163, v195, 0
	ds_write_b16 v238, v195 offset:32
	v_fma_mixlo_f16 v176, v163, v176, 0
	ds_write_b16 v238, v176 offset:34
	v_fma_mixlo_f16 v175, v163, v175, 0
	ds_write_b16 v238, v175 offset:36
	v_fma_mixlo_f16 v174, v163, v174, 0
	ds_write_b16 v238, v174 offset:38
	s_cmp_eq_u64 s[8:9], 0
	s_cbranch_scc1 .Lk4_stdone
	v_fma_mixlo_f16 v173, v163, v173, 0
	ds_write_b16 v238, v173 offset:40
	v_fma_mixlo_f16 v172, v163, v172, 0
	ds_write_b16 v238, v172 offset:42
	v_fma_mixlo_f16 v164, v163, v164, 0
	ds_write_b16 v238, v164 offset:44
	v_fma_mixlo_f16 v161, v163, v161, 0
	ds_write_b16 v238, v161 offset:46

.LBB3_222:
	s_waitcnt vmcnt(0)
	v_ashrrev_i32_e32 v238, 1, v189
	v_lshl_add_u32 v238, v238, 2, s90
	ds_write_b32 v238, v240
	ds_write_b32 v238, v244 offset:128
	ds_write_b32 v238, v248 offset:256
	ds_write_b32 v238, v252 offset:384
	v_and_b32_e32 v238, 1, v189
	v_lshl_or_b32 v240, v240, 1, v238
	v_lshl_or_b32 v244, v244, 1, v238
	v_lshl_or_b32 v248, v248, 1, v238
	v_lshl_or_b32 v252, v252, 1, v238
	v_lshlrev_b32_e32 v240, 4, v240
	v_lshlrev_b32_e32 v244, 4, v244
	v_lshlrev_b32_e32 v248, 4, v248
	v_lshlrev_b32_e32 v252, 4, v252
	global_load_dwordx4 v[240:243], v240, s[60:61]
	global_load_dwordx4 v[244:247], v244, s[60:61]
	global_load_dwordx4 v[248:251], v248, s[60:61]
	global_load_dwordx4 v[252:255], v252, s[60:61]
	s_add_i32 s0, s74, s86
	s_addk_i32 s0, 0x4000
	v_ashrrev_i32_e32 v227, 3, v189
	v_add_u32_e32 v227, s0, v227
	v_min_i32_e32 v227, 0xc34f, v227
	v_and_b32_e32 v238, 7, v189
	v_lshl_or_b32 v227, v227, 3, v238
	v_lshlrev_b32_e32 v227, 2, v227
	global_load_dword v227, v227, s[62:63]
	v_lshlrev_b32_e32 v0, 4, v168
	v_add_u32_e32 v165, 0xca00, v0
	v_mad_u32_u24 v166, v167, s69, v0
	v_add_u32_e32 v12, s66, v165
	s_waitcnt lgkmcnt(0)
	s_barrier
	ds_read_b128 v[16:19], v12
	ds_read_b128 v[20:23], v12 offset:32
	ds_read_b128 v[24:27], v12 offset:64
	ds_read_b128 v[28:31], v12 offset:96
	v_add_u32_e32 v169, s95, v166
	ds_read_b128 v[160:163], v169
	ds_read_b128 v[170:173], v169 offset:32
	s_waitcnt lgkmcnt(1)
	v_mfma_f32_32x32x16_f16 v[16:31], v[96:99], v[160:163], v[16:31]
	ds_read_b128 v[0:3], v12 offset:128
	ds_read_b128 v[4:7], v12 offset:160
	ds_read_b128 v[8:11], v12 offset:192
	ds_read_b128 v[12:15], v12 offset:224
	v_lshlrev_b32_e32 v168, 3, v168
	v_mad_u32_u24 v174, v167, s69, v168
	v_add_u32_e32 v167, s95, v174
	s_mov_b32 s8, 0xc34f
	s_waitcnt lgkmcnt(4)
	v_mfma_f32_32x32x16_f16 v[16:31], v[100:103], v[170:173], v[16:31]
	s_waitcnt lgkmcnt(0)
	v_mfma_f32_32x32x16_f16 v[0:15], v[112:115], v[160:163], v[0:15]
	ds_read_b128 v[160:163], v169 offset:64
	ds_read_b128 v[190:193], v169 offset:96
	s_waitcnt lgkmcnt(1)
	v_mfma_f32_32x32x16_f16 v[16:31], v[104:107], v[160:163], v[16:31]
	v_mfma_f32_32x32x16_f16 v[0:15], v[116:119], v[170:173], v[0:15]
	s_waitcnt lgkmcnt(0)
	v_mfma_f32_32x32x16_f16 v[16:31], v[108:111], v[190:193], v[16:31]
	v_mfma_f32_32x32x16_f16 v[0:15], v[120:123], v[160:163], v[0:15]
	s_nop 10
	v_max_f32_e32 v168, 0, v17
	v_max_f32_e32 v17, 0, v18
	v_max_f32_e32 v18, 0, v19
	v_max_f32_e32 v16, 0, v16
	v_max_f32_e32 v20, 0, v20
	v_max_f32_e32 v21, 0, v21
	v_cvt_pk_f16_f32 v17, v17, v18
	v_max_f32_e32 v18, 0, v22
	v_max_f32_e32 v19, 0, v23
	v_mfma_f32_32x32x16_f16 v[0:15], v[124:127], v[190:193], v[0:15]
	v_cvt_pk_f16_f32 v16, v16, v168
	v_cvt_pk_f16_f32 v19, v18, v19
	v_cvt_pk_f16_f32 v18, v20, v21
	ds_write2_b64 v167, v[16:17], v[18:19] offset1:2
	v_max_f32_e32 v18, 0, v25
	v_max_f32_e32 v17, 0, v26
	v_max_f32_e32 v19, 0, v27
	v_max_f32_e32 v16, 0, v24
	v_cvt_pk_f16_f32 v17, v17, v19
	v_cvt_pk_f16_f32 v16, v16, v18
	v_max_f32_e32 v20, 0, v29
	v_max_f32_e32 v18, 0, v28
	v_max_f32_e32 v19, 0, v30
	v_max_f32_e32 v21, 0, v31
	v_cvt_pk_f16_f32 v19, v19, v21
	v_cvt_pk_f16_f32 v18, v18, v20
	ds_write2_b64 v167, v[16:17], v[18:19] offset0:4 offset1:6
	v_max_f32_e32 v16, 0, v1
	v_max_f32_e32 v1, v2, v2
	v_max_f32_e32 v1, 0, v1
	v_max_f32_e32 v2, 0, v3
	v_cvt_pk_f16_f32 v1, v1, v2
	v_max_f32_e32 v2, v4, v4
	v_max_f32_e32 v4, 0, v5
	v_max_f32_e32 v0, 0, v0
	v_max_f32_e32 v2, 0, v2
	v_max_f32_e32 v3, 0, v6
	v_max_f32_e32 v5, 0, v7
	v_cvt_pk_f16_f32 v0, v0, v16
	v_cvt_pk_f16_f32 v3, v3, v5
	v_cvt_pk_f16_f32 v2, v2, v4
	ds_write2_b64 v167, v[0:1], v[2:3] offset0:8 offset1:10
	v_max_f32_e32 v2, 0, v9
	v_max_f32_e32 v1, 0, v10
	v_max_f32_e32 v3, 0, v11
	v_max_f32_e32 v0, 0, v8
	v_cvt_pk_f16_f32 v1, v1, v3
	v_cvt_pk_f16_f32 v0, v0, v2
	v_max_f32_e32 v4, 0, v13
	v_max_f32_e32 v2, 0, v12
	v_max_f32_e32 v3, 0, v14
	v_max_f32_e32 v5, 0, v15
	v_cvt_pk_f16_f32 v3, v3, v5
	v_cvt_pk_f16_f32 v2, v2, v4
	ds_write2_b64 v167, v[0:1], v[2:3] offset0:12 offset1:14
	v_add_u32_e32 v12, s64, v165
	ds_read_b128 v[16:19], v12
	ds_read_b128 v[20:23], v12 offset:32
	ds_read_b128 v[24:27], v12 offset:64
	ds_read_b128 v[28:31], v12 offset:96
	v_add_u32_e32 v165, s98, v166
	ds_read_b128 v[160:163], v165
	ds_read_b128 v[166:169], v165 offset:32
	ds_read_b128 v[0:3], v12 offset:128
	ds_read_b128 v[4:7], v12 offset:160
	ds_read_b128 v[8:11], v12 offset:192
	ds_read_b128 v[12:15], v12 offset:224
	s_waitcnt lgkmcnt(5)
	v_mfma_f32_32x32x16_f16 v[16:31], v[128:131], v[160:163], v[16:31]
	s_waitcnt lgkmcnt(0)
	v_mfma_f32_32x32x16_f16 v[0:15], v[144:147], v[160:163], v[0:15]
	v_mfma_f32_32x32x16_f16 v[16:31], v[132:135], v[166:169], v[16:31]
	v_mfma_f32_32x32x16_f16 v[0:15], v[148:151], v[166:169], v[0:15]
	ds_read_b128 v[160:163], v165 offset:64
	ds_read_b128 v[166:169], v165 offset:96
	s_waitcnt lgkmcnt(1)
	v_mfma_f32_32x32x16_f16 v[16:31], v[136:139], v[160:163], v[16:31]
	s_waitcnt lgkmcnt(0)
	v_mfma_f32_32x32x16_f16 v[16:31], v[140:143], v[166:169], v[16:31]
	v_mfma_f32_32x32x16_f16 v[0:15], v[152:155], v[160:163], v[0:15]
	s_nop 10
	v_max_f32_e32 v161, 0, v17
	v_max_f32_e32 v17, v18, v18
	v_max_f32_e32 v17, 0, v17
	v_max_f32_e32 v18, 0, v19
	v_cvt_pk_f16_f32 v17, v17, v18
	v_max_f32_e32 v18, v20, v20
	v_max_f32_e32 v20, 0, v21
	v_mfma_f32_32x32x16_f16 v[0:15], v[156:159], v[166:169], v[0:15]
	v_max_f32_e32 v16, 0, v16
	v_max_f32_e32 v18, 0, v18
	v_max_f32_e32 v19, 0, v22
	v_max_f32_e32 v21, 0, v23
	v_add_u32_e32 v160, s98, v174
	v_cvt_pk_f16_f32 v16, v16, v161
	v_cvt_pk_f16_f32 v19, v19, v21
	v_cvt_pk_f16_f32 v18, v18, v20
	ds_write2_b64 v160, v[16:17], v[18:19] offset1:2
	v_max_f32_e32 v18, 0, v25
	v_max_f32_e32 v17, 0, v26
	v_max_f32_e32 v19, 0, v27
	v_max_f32_e32 v16, 0, v24
	v_cvt_pk_f16_f32 v17, v17, v19
	v_cvt_pk_f16_f32 v16, v16, v18
	v_max_f32_e32 v20, 0, v29
	v_max_f32_e32 v18, 0, v28
	v_max_f32_e32 v19, 0, v30
	v_max_f32_e32 v21, 0, v31
	v_cvt_pk_f16_f32 v19, v19, v21
	v_cvt_pk_f16_f32 v18, v18, v20
	ds_write2_b64 v160, v[16:17], v[18:19] offset0:4 offset1:6
	v_max_f32_e32 v16, 0, v1
	v_max_f32_e32 v1, v2, v2
	v_max_f32_e32 v1, 0, v1
	v_max_f32_e32 v2, 0, v3
	v_cvt_pk_f16_f32 v1, v1, v2
	v_max_f32_e32 v2, v4, v4
	v_max_f32_e32 v4, 0, v5
	v_max_f32_e32 v0, 0, v0
	v_max_f32_e32 v2, 0, v2
	v_max_f32_e32 v3, 0, v6
	v_max_f32_e32 v5, 0, v7
	v_cvt_pk_f16_f32 v0, v0, v16
	v_cvt_pk_f16_f32 v3, v3, v5
	v_cvt_pk_f16_f32 v2, v2, v4
	ds_write2_b64 v160, v[0:1], v[2:3] offset0:8 offset1:10
	v_max_f32_e32 v2, 0, v9
	v_max_f32_e32 v1, 0, v10
	v_max_f32_e32 v3, 0, v11
	v_max_f32_e32 v0, 0, v8
	v_cvt_pk_f16_f32 v1, v1, v3
	v_cvt_pk_f16_f32 v0, v0, v2
	v_max_f32_e32 v4, 0, v13
	v_max_f32_e32 v2, 0, v12
	v_max_f32_e32 v3, 0, v14
	v_max_f32_e32 v5, 0, v15
	v_cvt_pk_f16_f32 v3, v3, v5
	v_cvt_pk_f16_f32 v2, v2, v4
	v_mad_u32_u24 v12, v195, s69, v196
	ds_write2_b64 v160, v[0:1], v[2:3] offset0:12 offset1:14
	s_waitcnt lgkmcnt(0)
	s_barrier
	v_mul_u32_u24_e32 v16, 0x410, v195
	v_add_u32_e32 v16, v196, v16
	ds_read_b128 v[8:11], v16
	ds_read_b128 v[12:15], v16 offset:16640
	ds_read_b128 v[20:23], v16 offset:64
	ds_read_b128 v[24:27], v16 offset:16704
	ds_read_b128 v[28:31], v16 offset:128
	ds_read_b128 v[160:163], v16 offset:16768
	ds_read_b128 v[164:167], v16 offset:192
	ds_read_b128 v[168:171], v16 offset:16832
	s_waitcnt lgkmcnt(7)
	v_mfma_f32_16x16x32_f16 v[0:3], v[32:35], v[8:11], 0
	ds_read_b128 v[8:11], v16 offset:256
	s_waitcnt lgkmcnt(7)
	v_mfma_f32_16x16x32_f16 v[4:7], v[32:35], v[12:15], 0
	ds_read_b128 v[12:15], v16 offset:16896
	s_waitcnt lgkmcnt(7)
	v_mfma_f32_16x16x32_f16 v[0:3], v[36:39], v[20:23], v[0:3]
	ds_read_b128 v[20:23], v16 offset:320
	s_waitcnt lgkmcnt(7)
	v_mfma_f32_16x16x32_f16 v[4:7], v[36:39], v[24:27], v[4:7]
	ds_read_b128 v[24:27], v16 offset:16960
	s_waitcnt lgkmcnt(7)
	v_mfma_f32_16x16x32_f16 v[0:3], v[40:43], v[28:31], v[0:3]
	ds_read_b128 v[28:31], v16 offset:384
	s_waitcnt lgkmcnt(7)
	v_mfma_f32_16x16x32_f16 v[4:7], v[40:43], v[160:163], v[4:7]
	ds_read_b128 v[160:163], v16 offset:17024
	s_waitcnt lgkmcnt(7)
	v_mfma_f32_16x16x32_f16 v[0:3], v[44:47], v[164:167], v[0:3]
	ds_read_b128 v[164:167], v16 offset:448
	s_waitcnt lgkmcnt(7)
	v_mfma_f32_16x16x32_f16 v[4:7], v[44:47], v[168:171], v[4:7]
	ds_read_b128 v[168:171], v16 offset:17088
	s_waitcnt lgkmcnt(7)
	v_mfma_f32_16x16x32_f16 v[0:3], v[56:59], v[8:11], v[0:3]
	ds_read_b128 v[8:11], v16 offset:512
	s_waitcnt lgkmcnt(7)
	v_mfma_f32_16x16x32_f16 v[4:7], v[56:59], v[12:15], v[4:7]
	ds_read_b128 v[12:15], v16 offset:17152
	s_waitcnt lgkmcnt(7)
	v_mfma_f32_16x16x32_f16 v[0:3], v[48:51], v[20:23], v[0:3]
	ds_read_b128 v[20:23], v16 offset:576
	s_waitcnt lgkmcnt(7)
	v_mfma_f32_16x16x32_f16 v[4:7], v[48:51], v[24:27], v[4:7]
	ds_read_b128 v[24:27], v16 offset:17216
	s_waitcnt lgkmcnt(7)
	v_mfma_f32_16x16x32_f16 v[0:3], v[52:55], v[28:31], v[0:3]
	ds_read_b128 v[28:31], v16 offset:640
	s_waitcnt lgkmcnt(7)
	v_mfma_f32_16x16x32_f16 v[4:7], v[52:55], v[160:163], v[4:7]
	ds_read_b128 v[160:163], v16 offset:17280
	s_waitcnt lgkmcnt(7)
	v_mfma_f32_16x16x32_f16 v[0:3], v[76:79], v[164:167], v[0:3]
	ds_read_b128 v[164:167], v16 offset:704
	s_waitcnt lgkmcnt(7)
	v_mfma_f32_16x16x32_f16 v[4:7], v[76:79], v[168:171], v[4:7]
	ds_read_b128 v[168:171], v16 offset:17344
	s_waitcnt lgkmcnt(7)
	v_mfma_f32_16x16x32_f16 v[0:3], v[60:63], v[8:11], v[0:3]
	ds_read_b128 v[8:11], v16 offset:768
	s_waitcnt lgkmcnt(7)
	v_mfma_f32_16x16x32_f16 v[4:7], v[60:63], v[12:15], v[4:7]
	ds_read_b128 v[12:15], v16 offset:17408
	s_waitcnt lgkmcnt(7)
	v_mfma_f32_16x16x32_f16 v[0:3], v[64:67], v[20:23], v[0:3]
	ds_read_b128 v[20:23], v16 offset:832
	s_waitcnt lgkmcnt(7)
	v_mfma_f32_16x16x32_f16 v[4:7], v[64:67], v[24:27], v[4:7]
	ds_read_b128 v[24:27], v16 offset:17472
	s_waitcnt lgkmcnt(7)
	v_mfma_f32_16x16x32_f16 v[0:3], v[68:71], v[28:31], v[0:3]
	ds_read_b128 v[28:31], v16 offset:896
	s_waitcnt lgkmcnt(7)
	v_mfma_f32_16x16x32_f16 v[4:7], v[68:71], v[160:163], v[4:7]
	ds_read_b128 v[160:163], v16 offset:17536
	s_waitcnt lgkmcnt(7)
	v_mfma_f32_16x16x32_f16 v[0:3], v[72:75], v[164:167], v[0:3]
	ds_read_b128 v[164:167], v16 offset:960
	s_waitcnt lgkmcnt(7)
	v_mfma_f32_16x16x32_f16 v[4:7], v[72:75], v[168:171], v[4:7]
	ds_read_b128 v[168:171], v16 offset:17600
	s_waitcnt lgkmcnt(7)
	v_mfma_f32_16x16x32_f16 v[0:3], v[80:83], v[8:11], v[0:3]
	s_waitcnt lgkmcnt(6)
	v_mfma_f32_16x16x32_f16 v[4:7], v[80:83], v[12:15], v[4:7]
	s_waitcnt lgkmcnt(5)
	v_mfma_f32_16x16x32_f16 v[0:3], v[84:87], v[20:23], v[0:3]
	s_waitcnt lgkmcnt(4)
	v_mfma_f32_16x16x32_f16 v[4:7], v[84:87], v[24:27], v[4:7]
	s_waitcnt lgkmcnt(3)
	v_mfma_f32_16x16x32_f16 v[0:3], v[88:91], v[28:31], v[0:3]
	s_waitcnt lgkmcnt(2)
	v_mfma_f32_16x16x32_f16 v[4:7], v[88:91], v[160:163], v[4:7]
	s_waitcnt lgkmcnt(1)
	v_mfma_f32_16x16x32_f16 v[0:3], v[92:95], v[164:167], v[0:3]
	s_waitcnt lgkmcnt(0)
	v_mfma_f32_16x16x32_f16 v[4:7], v[92:95], v[168:171], v[4:7]
	s_waitcnt vmcnt(0)
	v_lshl_add_u32 v238, v189, 4, s88
	ds_write_b128 v238, v[240:243]
	ds_write_b128 v238, v[244:247] offset:1024
	ds_write_b128 v238, v[248:251] offset:2048
	ds_write_b128 v238, v[252:255] offset:3072
	v_lshrrev_b32_e32 v17, 4, v189
	v_lshlrev_b32_e32 v17, 3, v17
	s_lshl_b32 s0, s3, 1
	v_add_u32_e32 v18, s74, v195
	v_lshl_add_u32 v17, v18, 7, v17
	v_add_u32_e32 v17, s0, v17
	v_readlane_b32 s4, v226, 0
	v_readlane_b32 s5, v226, 1
	s_mov_b32 s1, 0xc350
	v_add_u32_e32 v19, 16, v18
	v_lshlrev_b32_e32 v28, 2, v195
	s_nop 1
	v_cvt_pk_f16_f32 v20, v0, v1
	v_cvt_pk_f16_f32 v21, v2, v3
	v_cvt_pk_f16_f32 v22, v4, v5
	v_cvt_pk_f16_f32 v23, v6, v7
	v_cmp_gt_i32_e32 vcc, s1, v18
	v_cmp_gt_i32_e64 s[8:9], s1, v19
	v_mul_f32_e32 v24, v228, v0
	v_mul_f32_e32 v25, v232, v0
	v_mul_f32_e32 v26, v228, v4
	v_mul_f32_e32 v27, v232, v4
	v_fmac_f32_e32 v24, v229, v1
	v_fmac_f32_e32 v25, v233, v1
	v_fmac_f32_e32 v26, v229, v5
	v_fmac_f32_e32 v27, v233, v5
	v_fmac_f32_e32 v24, v230, v2
	v_fmac_f32_e32 v25, v234, v2
	v_fmac_f32_e32 v26, v230, v6
	v_fmac_f32_e32 v27, v234, v6
	v_fmac_f32_e32 v24, v231, v3
	v_fmac_f32_e32 v25, v235, v3
	v_fmac_f32_e32 v26, v231, v7
	v_fmac_f32_e32 v27, v235, v7
	s_mov_b64 exec, vcc
	global_store_dwordx2 v17, v[20:21], s[4:5]
	s_mov_b64 exec, s[8:9]
	global_store_dwordx2 v17, v[22:23], s[4:5] offset:2048
	s_mov_b64 exec, -1
	v_mov_b32_e32 v12, v24
	v_mov_b32_e32 v13, v25
	v_mov_b32_e32 v14, v26
	v_mov_b32_e32 v15, v27
	s_nop 1
	v_permlane32_swap_b32_e32 v24, v12
	v_permlane32_swap_b32_e32 v25, v13
	v_permlane32_swap_b32_e32 v26, v14
	v_permlane32_swap_b32_e32 v27, v15
	v_add_f32_e32 v24, v24, v12
	v_add_f32_e32 v25, v25, v13
	v_add_f32_e32 v26, v26, v14
	v_add_f32_e32 v27, v27, v15
	ds_swizzle_b32 v12, v24 offset:0x401f
	ds_swizzle_b32 v13, v25 offset:0x401f
	ds_swizzle_b32 v14, v26 offset:0x401f
	ds_swizzle_b32 v15, v27 offset:0x401f
	s_waitcnt lgkmcnt(0)
	v_add_f32_e32 v24, v24, v12
	v_add_f32_e32 v25, v25, v13
	v_add_f32_e32 v26, v26, v14
	v_add_f32_e32 v27, v27, v15
	s_lshl_b32 s0, s3, 4
	s_add_i32 s0, s0, 0xd3c0
	v_lshl_add_u32 v28, v195, 2, s0
	s_mov_b64 exec, 0xffff
	ds_write_b32 v28, v24
	ds_write_b32 v28, v26 offset:64
	ds_write_b32 v28, v25 offset:128
	ds_write_b32 v28, v27 offset:192
	s_mov_b64 exec, -1
	v_add_u32_e32 v1, s65, v189
	v_cmp_gt_i32_e32 vcc, 32, v1
	s_waitcnt lgkmcnt(0)
	s_barrier
	s_and_saveexec_b64 s[0:1], vcc
	s_cbranch_execz .LBB3_5
	v_add_u32_e32 v0, s74, v1
	s_mov_b32 s4, 0xc350
	v_lshlrev_b32_e32 v1, 2, v1
	v_cmp_gt_i32_e32 vcc, s4, v0
	v_add_u32_e32 v2, 0xd000, v1
	s_and_saveexec_b64 s[4:5], vcc
	s_cbranch_execz .LBB3_4
	v_add_u32_e32 v8, 0xd3c0, v1
	v_add_u32_e32 v9, 0xd440, v1
	ds_read2st64_b32 v[4:5], v8 offset1:1
	ds_read2st64_b32 v[10:11], v8 offset0:2 offset1:3
	ds_read2st64_b32 v[12:13], v9 offset1:1
	ds_read2st64_b32 v[14:15], v9 offset0:2 offset1:3
	v_ashrrev_i32_e32 v1, 31, v0
	v_readlane_b32 s8, v226, 0
	v_lshlrev_b64 v[0:1], 2, v[0:1]
	v_readlane_b32 s10, v226, 2
	v_readlane_b32 s11, v226, 3
	v_lshl_add_u64 v[6:7], s[76:77], 0, v[0:1]
	v_readlane_b32 s9, v226, 1
	v_lshl_add_u64 v[0:1], s[10:11], 0, v[0:1]
	s_waitcnt lgkmcnt(0)
	v_add_f32_e32 v5, v4, v5
	v_add_f32_e32 v10, v10, v11
	v_add_f32_e32 v4, v12, v13
	v_add_f32_e32 v12, v14, v15
	v_add_f32_e32 v5, v5, v10
	v_add_f32_e32 v4, v4, v12
	global_store_dword v[0:1], v5, off
	global_store_dword v[6:7], v4, off
	s_branch .LBB3_4

	.amdhsa_kernel _Z8k_layer1PKiS0_PKfS2_PK15HIP_vector_typeIjLj4EEPKDv8_DF16_S9_S2_S2_S2_PDF16_PfSB_
		.amdhsa_group_segment_fixed_size 55232
		.amdhsa_private_segment_fixed_size 0
		.amdhsa_kernarg_size 360
		.amdhsa_user_sgpr_count 2
		.amdhsa_user_sgpr_dispatch_ptr 0
		.amdhsa_user_sgpr_queue_ptr 0
		.amdhsa_user_sgpr_kernarg_segment_ptr 1
		.amdhsa_user_sgpr_dispatch_id 0
		.amdhsa_user_sgpr_kernarg_preload_length 0
		.amdhsa_user_sgpr_kernarg_preload_offset 0
		.amdhsa_user_sgpr_private_segment_size 0
		.amdhsa_uses_dynamic_stack 0
		.amdhsa_enable_private_segment 0
		.amdhsa_system_sgpr_workgroup_id_x 1
		.amdhsa_system_sgpr_workgroup_id_y 0
		.amdhsa_system_sgpr_workgroup_id_z 0
		.amdhsa_system_sgpr_workgroup_info 0
		.amdhsa_system_vgpr_workitem_id 0
		.amdhsa_next_free_vgpr 256
		.amdhsa_next_free_sgpr 100
		.amdhsa_accum_offset 256
		.amdhsa_reserve_vcc 1
		.amdhsa_float_round_mode_32 0
		.amdhsa_float_round_mode_16_64 0
		.amdhsa_float_denorm_mode_32 3
		.amdhsa_float_denorm_mode_16_64 3
		.amdhsa_dx10_clamp 1
		.amdhsa_ieee_mode 1
		.amdhsa_fp16_overflow 0
		.amdhsa_tg_split 0
		.amdhsa_exception_fp_ieee_invalid_op 0
		.amdhsa_exception_fp_denorm_src 0
		.amdhsa_exception_fp_ieee_div_zero 0
		.amdhsa_exception_fp_ieee_overflow 0
		.amdhsa_exception_fp_ieee_underflow 0
		.amdhsa_exception_fp_ieee_inexact 0
		.amdhsa_exception_int_div_zero 0
	.end_amdhsa_kernel

amdhsa.kernels:
  - .agpr_count:     0
    .args:
      - .actual_access:  read_only
        .address_space:  global
        .offset:         0
        .size:           8
        .value_kind:     global_buffer
      - .actual_access:  read_only
        .address_space:  global
        .offset:         8
        .size:           8
        .value_kind:     global_buffer
      - .actual_access:  read_only
        .address_space:  global
        .offset:         16
        .size:           8
        .value_kind:     global_buffer
      - .actual_access:  read_only
        .address_space:  global
        .offset:         24
        .size:           8
        .value_kind:     global_buffer
      - .actual_access:  read_only
        .address_space:  global
        .offset:         32
        .size:           8
        .value_kind:     global_buffer
      - .actual_access:  write_only
        .address_space:  global
        .offset:         40
        .size:           8
        .value_kind:     global_buffer
      - .actual_access:  write_only
        .address_space:  global
        .offset:         48
        .size:           8
        .value_kind:     global_buffer
      - .actual_access:  write_only
        .address_space:  global
        .offset:         56
        .size:           8
        .value_kind:     global_buffer
      - .actual_access:  write_only
        .address_space:  global
        .offset:         64
        .size:           8
        .value_kind:     global_buffer
    .group_segment_fixed_size: 1024
    .kernarg_segment_align: 8
    .kernarg_segment_size: 72
    .language:       OpenCL C
    .language_version:
      - 2
      - 0
    .max_flat_workgroup_size: 512
    .name:           _Z11k_hist_prepPKiPKfS2_S2_S2_PiPfPDF16_S5_
    .private_segment_fixed_size: 0
    .sgpr_count:     20
    .sgpr_spill_count: 0
    .symbol:         _Z11k_hist_prepPKiPKfS2_S2_S2_PiPfPDF16_S5_.kd
    .uniform_work_group_size: 1
    .uses_dynamic_stack: false
    .vgpr_count:     42
    .vgpr_spill_count: 0
    .wavefront_size: 64
  - .agpr_count:     0
    .args:
      - .actual_access:  read_only
        .address_space:  global
        .offset:         0
        .size:           8
        .value_kind:     global_buffer
      - .actual_access:  read_only
        .address_space:  global
        .offset:         8
        .size:           8
        .value_kind:     global_buffer
      - .actual_access:  write_only
        .address_space:  global
        .offset:         16
        .size:           8
        .value_kind:     global_buffer
      - .actual_access:  write_only
        .address_space:  global
        .offset:         24
        .size:           8
        .value_kind:     global_buffer
      - .actual_access:  read_only
        .address_space:  global
        .offset:         32
        .size:           8
        .value_kind:     global_buffer
      - .actual_access:  read_only
        .address_space:  global
        .offset:         40
        .size:           8
        .value_kind:     global_buffer
      - .actual_access:  write_only
        .address_space:  global
        .offset:         48
        .size:           8
        .value_kind:     global_buffer
      - .actual_access:  write_only
        .address_space:  global
        .offset:         56
        .size:           8
        .value_kind:     global_buffer
      - .actual_access:  write_only
        .address_space:  global
        .offset:         64
        .size:           8
        .value_kind:     global_buffer
    .group_segment_fixed_size: 9344
    .kernarg_segment_align: 8
    .kernarg_segment_size: 72
    .language:       OpenCL C
    .language_version:
      - 2
      - 0
    .max_flat_workgroup_size: 512
    .name:           _Z14k_scatter_nodePKiS0_PjPiPKfS4_PfS5_PDF16_
    .private_segment_fixed_size: 0
    .sgpr_count:     106
    .sgpr_spill_count: 10
    .symbol:         _Z14k_scatter_nodePKiS0_PjPiPKfS4_PfS5_PDF16_.kd
    .uniform_work_group_size: 1
    .uses_dynamic_stack: false
    .vgpr_count:     118
    .vgpr_spill_count: 0
    .wavefront_size: 64
  - .agpr_count:     0
    .args:
      - .actual_access:  read_only
        .address_space:  global
        .offset:         0
        .size:           8
        .value_kind:     global_buffer
      - .actual_access:  read_only
        .address_space:  global
        .offset:         8
        .size:           8
        .value_kind:     global_buffer
      - .actual_access:  write_only
        .address_space:  global
        .offset:         16
        .size:           8
        .value_kind:     global_buffer
      - .actual_access:  write_only
        .address_space:  global
        .offset:         24
        .size:           8
        .value_kind:     global_buffer
    .group_segment_fixed_size: 3072
    .kernarg_segment_align: 8
    .kernarg_segment_size: 32
    .language:       OpenCL C
    .language_version:
      - 2
      - 0
    .max_flat_workgroup_size: 1024
    .name:           _Z5k_csrPKjPKiPiS3_
    .private_segment_fixed_size: 0
    .sgpr_count:     34
    .sgpr_spill_count: 0
    .symbol:         _Z5k_csrPKjPKiPiS3_.kd
    .uniform_work_group_size: 1
    .uses_dynamic_stack: false
    .vgpr_count:     18
    .vgpr_spill_count: 0
    .wavefront_size: 64
  - .agpr_count:     0
    .args:
      - .actual_access:  read_only
        .address_space:  global
        .offset:         0
        .size:           8
        .value_kind:     global_buffer
      - .actual_access:  read_only
        .address_space:  global
        .offset:         8
        .size:           8
        .value_kind:     global_buffer
      - .actual_access:  read_only
        .address_space:  global
        .offset:         16
        .size:           8
        .value_kind:     global_buffer
      - .actual_access:  read_only
        .address_space:  global
        .offset:         24
        .size:           8
        .value_kind:     global_buffer
      - .actual_access:  read_only
        .address_space:  global
        .offset:         32
        .size:           8
        .value_kind:     global_buffer
      - .actual_access:  read_only
        .address_space:  global
        .offset:         40
        .size:           8
        .value_kind:     global_buffer
      - .actual_access:  read_only
        .address_space:  global
        .offset:         48
        .size:           8
        .value_kind:     global_buffer
      - .actual_access:  read_only
        .address_space:  global
        .offset:         56
        .size:           8
        .value_kind:     global_buffer
      - .actual_access:  read_only
        .address_space:  global
        .offset:         64
        .size:           8
        .value_kind:     global_buffer
      - .actual_access:  read_only
        .address_space:  global
        .offset:         72
        .size:           8
        .value_kind:     global_buffer
      - .actual_access:  write_only
        .address_space:  global
        .offset:         80
        .size:           8
        .value_kind:     global_buffer
      - .actual_access:  write_only
        .address_space:  global
        .offset:         88
        .size:           8
        .value_kind:     global_buffer
      - .actual_access:  write_only
        .address_space:  global
        .offset:         96
        .size:           8
        .value_kind:     global_buffer
      - .offset:         104
        .size:           4
        .value_kind:     hidden_block_count_x
      - .offset:         108
        .size:           4
        .value_kind:     hidden_block_count_y
      - .offset:         112
        .size:           4
        .value_kind:     hidden_block_count_z
      - .offset:         116
        .size:           2
        .value_kind:     hidden_group_size_x
      - .offset:         118
        .size:           2
        .value_kind:     hidden_group_size_y
      - .offset:         120
        .size:           2
        .value_kind:     hidden_group_size_z
      - .offset:         122
        .size:           2
        .value_kind:     hidden_remainder_x
      - .offset:         124
        .size:           2
        .value_kind:     hidden_remainder_y
      - .offset:         126
        .size:           2
        .value_kind:     hidden_remainder_z
      - .offset:         144
        .size:           8
        .value_kind:     hidden_global_offset_x
      - .offset:         152
        .size:           8
        .value_kind:     hidden_global_offset_y
      - .offset:         160
        .size:           8
        .value_kind:     hidden_global_offset_z
      - .offset:         168
        .size:           2
        .value_kind:     hidden_grid_dims
    .group_segment_fixed_size: 55232
    .kernarg_segment_align: 8
    .kernarg_segment_size: 360
    .language:       OpenCL C
    .language_version:
      - 2
      - 0
    .max_flat_workgroup_size: 256
    .name:           _Z8k_layer1PKiS0_PKfS2_PK15HIP_vector_typeIjLj4EEPKDv8_DF16_S9_S2_S2_S2_PDF16_PfSB_
    .private_segment_fixed_size: 0
    .sgpr_count:     106
    .sgpr_spill_count: 7
    .symbol:         _Z8k_layer1PKiS0_PKfS2_PK15HIP_vector_typeIjLj4EEPKDv8_DF16_S9_S2_S2_S2_PDF16_PfSB_.kd
    .uniform_work_group_size: 1
    .uses_dynamic_stack: false
    .vgpr_count:     256
    .vgpr_spill_count: 0
    .wavefront_size: 64
  - .agpr_count:     0
    .args:
      - .actual_access:  read_only
        .address_space:  global
        .offset:         0
        .size:           8
        .value_kind:     global_buffer
      - .actual_access:  read_only
        .address_space:  global
        .offset:         8
        .size:           8
        .value_kind:     global_buffer
      - .actual_access:  read_only
        .address_space:  global
        .offset:         16
        .size:           8
        .value_kind:     global_buffer
      - .actual_access:  read_only
        .address_space:  global
        .offset:         24
        .size:           8
        .value_kind:     global_buffer
      - .actual_access:  read_only
        .address_space:  global
        .offset:         32
        .size:           8
        .value_kind:     global_buffer
      - .actual_access:  read_only
        .address_space:  global
        .offset:         40
        .size:           8
        .value_kind:     global_buffer
      - .actual_access:  write_only
        .address_space:  global
        .offset:         48
        .size:           8
        .value_kind:     global_buffer
    .group_segment_fixed_size: 0
    .kernarg_segment_align: 8
    .kernarg_segment_size: 56
    .language:       OpenCL C
    .language_version:
      - 2
      - 0
    .max_flat_workgroup_size: 256
    .name:           _Z8k_layer2PKiS0_PKfS2_PK15HIP_vector_typeIjLj4EES2_Pf
    .private_segment_fixed_size: 0
    .sgpr_count:     52
    .sgpr_spill_count: 0
    .symbol:         _Z8k_layer2PKiS0_PKfS2_PK15HIP_vector_typeIjLj4EES2_Pf.kd
    .uniform_work_group_size: 1
    .uses_dynamic_stack: false
    .vgpr_count:     70
    .vgpr_spill_count: 0
    .wavefront_size: 64
